# v26 + v_fma_mix_f32 peephole (cvt+pk_fma -> fma_mix, same f32 fused math) in agg1g2, agg2, readout accumulate code
# speedup vs baseline: 1.0012x; 1.0012x over previous
.LBB2_6:
	s_or_b64 exec, exec, s[10:11]
	ds_read2_b32 v[10:11], v51 offset1:4
	s_lshl_b32 s10, s33, 21
	s_waitcnt lgkmcnt(7)
	ds_read2_b32 v[12:13], v51 offset0:8 offset1:12
	s_add_u32 s34, s16, s10
	s_addc_u32 s35, s17, 0
	s_waitcnt lgkmcnt(1)
	v_lshl_add_u32 v10, v10, 7, v110
	v_lshl_add_u32 v11, v11, 7, v110
	global_load_dwordx4 v[42:45], v10, s[34:35]
	global_load_dwordx4 v[38:41], v11, s[34:35]
	ds_read2_b32 v[14:15], v51 offset0:16 offset1:20
	s_waitcnt lgkmcnt(1)
	v_lshl_add_u32 v10, v12, 7, v110
	global_load_dwordx4 v[30:33], v10, s[34:35]
	v_lshl_add_u32 v10, v13, 7, v110
	global_load_dwordx4 v[26:29], v10, s[34:35]
	s_waitcnt lgkmcnt(0)
	v_lshl_add_u32 v10, v14, 7, v110
	global_load_dwordx4 v[10:13], v10, s[34:35]
	v_lshl_add_u32 v14, v15, 7, v110
	global_load_dwordx4 v[14:17], v14, s[34:35]
	ds_read2_b32 v[92:93], v114 offset1:4
	ds_read2_b32 v[18:19], v51 offset0:24 offset1:28
	ds_read2_b32 v[90:91], v114 offset0:8 offset1:12
	ds_read2_b32 v[20:21], v51 offset0:32 offset1:36
	ds_read2_b32 v[94:95], v114 offset0:16 offset1:20
	s_waitcnt lgkmcnt(3)
	v_lshl_add_u32 v18, v18, 7, v110
	v_lshl_add_u32 v19, v19, 7, v110
	s_waitcnt lgkmcnt(1)
	v_lshl_add_u32 v20, v20, 7, v110
	v_lshl_add_u32 v22, v21, 7, v110
	global_load_dwordx4 v[46:49], v18, s[34:35]
	global_load_dwordx4 v[34:37], v19, s[34:35]
	s_nop 0
	global_load_dwordx4 v[18:21], v20, s[34:35]
	s_nop 0
	global_load_dwordx4 v[22:25], v22, s[34:35]
	v_mov_b32_e32 v96, v93
	v_mov_b32_e32 v97, v92
	v_mov_b32_e32 v60, v93
	v_mov_b32_e32 v100, v91
	v_mov_b32_e32 v98, v91
	v_mov_b32_e32 v99, v90
	s_waitcnt vmcnt(9)
	v_cvt_f32_f16_sdwa v103, v45 dst_sel:DWORD dst_unused:UNUSED_PAD src0_sel:WORD_1
	s_waitcnt vmcnt(8)
	v_cvt_f32_f16_sdwa v102, v41 dst_sel:DWORD dst_unused:UNUSED_PAD src0_sel:WORD_1
	v_cvt_f32_f16_e32 v106, v42
	v_cvt_f32_f16_sdwa v107, v42 dst_sel:DWORD dst_unused:UNUSED_PAD src0_sel:WORD_1
	v_cvt_f32_f16_e32 v116, v38
	v_cvt_f32_f16_sdwa v117, v38 dst_sel:DWORD dst_unused:UNUSED_PAD src0_sel:WORD_1
	v_cvt_f32_f16_e32 v122, v44
	v_cvt_f32_f16_sdwa v123, v44 dst_sel:DWORD dst_unused:UNUSED_PAD src0_sel:WORD_1
	v_cvt_f32_f16_e32 v53, v45
	s_waitcnt vmcnt(7)
	v_cvt_f32_f16_e32 v118, v30
	v_cvt_f32_f16_sdwa v119, v30 dst_sel:DWORD dst_unused:UNUSED_PAD src0_sel:WORD_1
	v_cvt_f32_f16_e32 v44, v40
	v_cvt_f32_f16_sdwa v45, v40 dst_sel:DWORD dst_unused:UNUSED_PAD src0_sel:WORD_1
	v_cvt_f32_f16_e32 v101, v41
	s_waitcnt vmcnt(6)
	v_cvt_f32_f16_e32 v120, v26
	v_cvt_f32_f16_sdwa v121, v26 dst_sel:DWORD dst_unused:UNUSED_PAD src0_sel:WORD_1
	v_cvt_f32_f16_e32 v40, v32
	v_cvt_f32_f16_sdwa v41, v32 dst_sel:DWORD dst_unused:UNUSED_PAD src0_sel:WORD_1
	v_cvt_f32_f16_e32 v124, v33
	v_cvt_f32_f16_sdwa v105, v33 dst_sel:DWORD dst_unused:UNUSED_PAD src0_sel:WORD_1
	v_cvt_f32_f16_sdwa v104, v29 dst_sel:DWORD dst_unused:UNUSED_PAD src0_sel:WORD_1
	v_cvt_f32_f16_e32 v32, v28
	v_cvt_f32_f16_sdwa v33, v28 dst_sel:DWORD dst_unused:UNUSED_PAD src0_sel:WORD_1
	v_cvt_f32_f16_e32 v125, v29
	s_waitcnt vmcnt(5)
	v_cvt_f32_f16_e32 v28, v10
	v_cvt_f32_f16_sdwa v29, v10 dst_sel:DWORD dst_unused:UNUSED_PAD src0_sel:WORD_1
	v_pk_mul_f32 v[96:97], v[96:97], v[102:103]
	v_cvt_f32_f16_e32 v102, v12
	v_cvt_f32_f16_sdwa v103, v12 dst_sel:DWORD dst_unused:UNUSED_PAD src0_sel:WORD_1
	v_cvt_f32_f16_e32 v12, v13
	v_fma_mix_f32 v42, v92, v43, v86 op_sel_hi:[0,1,0]
	v_fma_mix_f32 v43, v92, v43, v87 op_sel:[0,1,0] op_sel_hi:[0,1,0]
	v_pk_fma_f32 v[84:85], v[92:93], v[122:123], v[84:85] op_sel_hi:[0,1,1]
	v_fma_mix_f32 v38, v60, v39, v42 op_sel_hi:[0,1,0]
	v_fma_mix_f32 v39, v60, v39, v43 op_sel:[0,1,0] op_sel_hi:[0,1,0]
	v_pk_fma_f32 v[42:43], v[60:61], v[44:45], v[84:85] op_sel_hi:[0,1,1]
	v_fma_mix_f32 v30, v90, v31, v38 op_sel_hi:[0,1,0]
	v_fma_mix_f32 v31, v90, v31, v39 op_sel:[0,1,0] op_sel_hi:[0,1,0]
	v_pk_fma_f32 v[38:39], v[90:91], v[40:41], v[42:43] op_sel_hi:[0,1,1]
	v_fma_mix_f32 v26, v100, v27, v30 op_sel_hi:[0,1,0]
	v_fma_mix_f32 v27, v100, v27, v31 op_sel:[0,1,0] op_sel_hi:[0,1,0]
	s_waitcnt lgkmcnt(0)
	v_fma_mix_f32 v26, v94, v11, v26 op_sel_hi:[0,1,0]
	v_fma_mix_f32 v27, v94, v11, v27 op_sel:[0,1,0] op_sel_hi:[0,1,0]
	v_pk_fma_f32 v[10:11], v[100:101], v[32:33], v[38:39] op_sel_hi:[0,1,1]
	v_mul_f32_e32 v32, v94, v12
	v_cvt_f32_f16_sdwa v13, v13 dst_sel:DWORD dst_unused:UNUSED_PAD src0_sel:WORD_1
	s_waitcnt vmcnt(4)
	v_cvt_f32_f16_sdwa v12, v17 dst_sel:DWORD dst_unused:UNUSED_PAD src0_sel:WORD_1
	v_mul_f32_e32 v86, v92, v53
	v_pk_fma_f32 v[30:31], v[94:95], v[102:103], v[10:11] op_sel_hi:[0,1,1]
	v_cvt_f32_f16_e32 v42, v16
	v_cvt_f32_f16_e32 v10, v17
	v_cvt_f32_f16_sdwa v43, v16 dst_sel:DWORD dst_unused:UNUSED_PAD src0_sel:WORD_1
	v_mov_b32_e32 v16, v95
	v_mov_b32_e32 v17, v94
	v_mov_b32_e32 v87, v97
	v_pk_mul_f32 v[98:99], v[98:99], v[104:105]
	v_pk_fma_f32 v[88:89], v[92:93], v[106:107], v[88:89] op_sel_hi:[0,1,1]
	v_mul_f32_e32 v92, v93, v101
	v_pk_mul_f32 v[12:13], v[16:17], v[12:13]
	v_pk_add_f32 v[16:17], v[82:83], v[86:87]
	v_mov_b32_e32 v93, v96
	v_mul_f32_e32 v104, v90, v124
	v_pk_add_f32 v[16:17], v[92:93], v[16:17]
	v_mov_b32_e32 v105, v99
	v_mul_f32_e32 v106, v91, v125
	v_pk_fma_f32 v[88:89], v[60:61], v[116:117], v[88:89] op_sel_hi:[0,1,1]
	v_cvt_f32_f16_e32 v38, v14
	v_cvt_f32_f16_sdwa v39, v14 dst_sel:DWORD dst_unused:UNUSED_PAD src0_sel:WORD_1
	v_pk_add_f32 v[16:17], v[104:105], v[16:17]
	v_mov_b32_e32 v107, v98
	v_pk_fma_f32 v[44:45], v[90:91], v[118:119], v[88:89] op_sel_hi:[0,1,1]
	v_pk_add_f32 v[16:17], v[106:107], v[16:17]
	v_mov_b32_e32 v33, v13
	v_pk_fma_f32 v[40:41], v[100:101], v[120:121], v[44:45] op_sel_hi:[0,1,1]
	v_pk_add_f32 v[16:17], v[32:33], v[16:17]
	ds_read2_b32 v[32:33], v114 offset0:24 offset1:28
	v_pk_fma_f32 v[28:29], v[94:95], v[28:29], v[40:41] op_sel_hi:[0,1,1]
	v_mov_b32_e32 v14, v95
	s_waitcnt vmcnt(3)
	ds_read2_b32 v[88:89], v114 offset0:32 offset1:36
	v_pk_fma_f32 v[28:29], v[14:15], v[38:39], v[28:29] op_sel_hi:[0,1,1]
	s_waitcnt vmcnt(2)
	s_waitcnt vmcnt(1)
	v_mul_f32_e32 v10, v95, v10
	s_waitcnt vmcnt(0)
	s_waitcnt lgkmcnt(1)
	v_fma_mix_f32 v28, v32, v46, v28 op_sel_hi:[0,1,0]
	v_fma_mix_f32 v29, v32, v46, v29 op_sel:[0,1,0] op_sel_hi:[0,1,0]
	v_mov_b32_e32 v44, v33
	v_fma_mix_f32 v28, v44, v34, v28 op_sel_hi:[0,1,0]
	v_fma_mix_f32 v29, v44, v34, v29 op_sel:[0,1,0] op_sel_hi:[0,1,0]
	s_waitcnt lgkmcnt(0)
	v_fma_mix_f32 v28, v88, v18, v28 op_sel_hi:[0,1,0]
	v_fma_mix_f32 v29, v88, v18, v29 op_sel:[0,1,0] op_sel_hi:[0,1,0]
	v_mov_b32_e32 v18, v89
	v_fma_mix_f32 v38, v18, v22, v28 op_sel_hi:[0,1,0]
	v_fma_mix_f32 v39, v18, v22, v29 op_sel:[0,1,0] op_sel_hi:[0,1,0]
	v_cvt_f32_f16_e32 v11, v49
	v_fma_mix_f32 v26, v14, v15, v26 op_sel_hi:[0,1,0]
	v_fma_mix_f32 v27, v14, v15, v27 op_sel:[0,1,0] op_sel_hi:[0,1,0]
	v_fma_mix_f32 v26, v32, v47, v26 op_sel_hi:[0,1,0]
	v_fma_mix_f32 v27, v32, v47, v27 op_sel:[0,1,0] op_sel_hi:[0,1,0]
	v_fma_mix_f32 v26, v44, v35, v26 op_sel_hi:[0,1,0]
	v_fma_mix_f32 v27, v44, v35, v27 op_sel:[0,1,0] op_sel_hi:[0,1,0]
	v_cvt_f32_f16_e32 v82, v48
	v_cvt_f32_f16_sdwa v83, v48 dst_sel:DWORD dst_unused:UNUSED_PAD src0_sel:WORD_1
	v_fma_mix_f32 v26, v88, v19, v26 op_sel_hi:[0,1,0]
	v_fma_mix_f32 v27, v88, v19, v27 op_sel:[0,1,0] op_sel_hi:[0,1,0]
	v_mul_f32_e32 v48, v32, v11
	v_cvt_f32_f16_sdwa v87, v49 dst_sel:DWORD dst_unused:UNUSED_PAD src0_sel:WORD_1
	v_cvt_f32_f16_sdwa v86, v37 dst_sel:DWORD dst_unused:UNUSED_PAD src0_sel:WORD_1
	v_cvt_f32_f16_e32 v11, v21
	v_fma_mix_f32 v34, v18, v23, v26 op_sel_hi:[0,1,0]
	v_fma_mix_f32 v35, v18, v23, v27 op_sel:[0,1,0] op_sel_hi:[0,1,0]
	v_pk_fma_f32 v[14:15], v[14:15], v[42:43], v[30:31] op_sel_hi:[0,1,1]
	v_mov_b32_e32 v90, v33
	v_mov_b32_e32 v91, v32
	v_pk_fma_f32 v[14:15], v[32:33], v[82:83], v[14:15] op_sel_hi:[0,1,1]
	v_pk_mul_f32 v[86:87], v[90:91], v[86:87]
	v_mul_f32_e32 v90, v88, v11
	v_fma_mix_f32 v14, v44, v36, v14 op_sel_hi:[0,1,0]
	v_fma_mix_f32 v15, v44, v36, v15 op_sel:[0,1,0] op_sel_hi:[0,1,0]
	v_cvt_f32_f16_e32 v11, v25
	v_fma_mix_f32 v14, v88, v20, v14 op_sel_hi:[0,1,0]
	v_fma_mix_f32 v15, v88, v20, v15 op_sel:[0,1,0] op_sel_hi:[0,1,0]
	v_cvt_f32_f16_e32 v13, v37
	v_fma_mix_f32 v36, v18, v24, v14 op_sel_hi:[0,1,0]
	v_fma_mix_f32 v37, v18, v24, v15 op_sel:[0,1,0] op_sel_hi:[0,1,0]
	v_cvt_f32_f16_sdwa v15, v21 dst_sel:DWORD dst_unused:UNUSED_PAD src0_sel:WORD_1
	v_cvt_f32_f16_sdwa v14, v25 dst_sel:DWORD dst_unused:UNUSED_PAD src0_sel:WORD_1
	v_mul_f32_e32 v18, v89, v11
	v_mov_b32_e32 v11, v12
	v_mov_b32_e32 v20, v89
	v_mov_b32_e32 v21, v88
	v_pk_add_f32 v[10:11], v[10:11], v[16:17]
	v_mov_b32_e32 v49, v87
	v_mul_f32_e32 v84, v33, v13
	v_pk_mul_f32 v[14:15], v[20:21], v[14:15]
	v_pk_add_f32 v[10:11], v[48:49], v[10:11]
	v_mov_b32_e32 v85, v86
	v_pk_add_f32 v[10:11], v[84:85], v[10:11]
	v_mov_b32_e32 v91, v15
	v_pk_add_f32 v[10:11], v[90:91], v[10:11]
	v_mov_b32_e32 v19, v14
	v_pk_add_f32 v[40:41], v[18:19], v[10:11]
	s_and_saveexec_b64 s[10:11], s[2:3]
	s_cbranch_execz .LBB2_8
	ds_read2_b32 v[10:11], v51 offset0:40 offset1:44
	ds_read2_b32 v[12:13], v51 offset0:48 offset1:52
	ds_read2_b32 v[14:15], v51 offset0:56 offset1:60
	s_waitcnt lgkmcnt(2)
	v_lshl_add_u32 v10, v10, 7, v110
	v_lshl_add_u32 v11, v11, 7, v110
	global_load_dwordx4 v[30:33], v10, s[34:35]
	global_load_dwordx4 v[26:29], v11, s[34:35]
	s_waitcnt lgkmcnt(1)
	v_lshl_add_u32 v10, v12, 7, v110
	v_lshl_add_u32 v11, v13, 7, v110
	global_load_dwordx4 v[22:25], v10, s[34:35]
	global_load_dwordx4 v[18:21], v11, s[34:35]
	s_waitcnt lgkmcnt(0)
	v_lshl_add_u32 v10, v14, 7, v110
	global_load_dwordx4 v[10:13], v10, s[34:35]
	v_lshl_add_u32 v14, v15, 7, v110
	global_load_dwordx4 v[14:17], v14, s[34:35]
	ds_read2_b32 v[44:45], v114 offset0:40 offset1:44
	ds_read2_b32 v[42:43], v114 offset0:48 offset1:52
	ds_read2_b32 v[46:47], v114 offset0:56 offset1:60
	s_waitcnt lgkmcnt(2)
	v_mov_b32_e32 v84, v45
	v_mov_b32_e32 v85, v44
	v_mov_b32_e32 v60, v45
	s_waitcnt lgkmcnt(1)
	v_mov_b32_e32 v82, v43
	v_mov_b32_e32 v83, v42
	v_mov_b32_e32 v86, v43
	s_waitcnt lgkmcnt(0)
	v_mov_b32_e32 v48, v47
	s_waitcnt vmcnt(5)
	v_cvt_f32_f16_e32 v92, v30
	v_cvt_f32_f16_sdwa v93, v30 dst_sel:DWORD dst_unused:UNUSED_PAD src0_sel:WORD_1
	v_cvt_f32_f16_e32 v104, v32
	v_cvt_f32_f16_sdwa v105, v32 dst_sel:DWORD dst_unused:UNUSED_PAD src0_sel:WORD_1
	v_cvt_f32_f16_e32 v49, v33
	v_cvt_f32_f16_sdwa v89, v33 dst_sel:DWORD dst_unused:UNUSED_PAD src0_sel:WORD_1
	s_waitcnt vmcnt(4)
	v_cvt_f32_f16_sdwa v88, v29 dst_sel:DWORD dst_unused:UNUSED_PAD src0_sel:WORD_1
	v_cvt_f32_f16_e32 v94, v26
	v_cvt_f32_f16_sdwa v95, v26 dst_sel:DWORD dst_unused:UNUSED_PAD src0_sel:WORD_1
	v_cvt_f32_f16_e32 v32, v28
	v_cvt_f32_f16_sdwa v33, v28 dst_sel:DWORD dst_unused:UNUSED_PAD src0_sel:WORD_1
	v_cvt_f32_f16_e32 v53, v29
	s_waitcnt vmcnt(3)
	v_cvt_f32_f16_e32 v96, v22
	v_cvt_f32_f16_sdwa v97, v22 dst_sel:DWORD dst_unused:UNUSED_PAD src0_sel:WORD_1
	v_cvt_f32_f16_e32 v28, v24
	v_cvt_f32_f16_sdwa v29, v24 dst_sel:DWORD dst_unused:UNUSED_PAD src0_sel:WORD_1
	v_cvt_f32_f16_e32 v87, v25
	s_waitcnt vmcnt(2)
	v_cvt_f32_f16_e32 v117, v21
	v_cvt_f32_f16_sdwa v91, v25 dst_sel:DWORD dst_unused:UNUSED_PAD src0_sel:WORD_1
	v_cvt_f32_f16_sdwa v90, v21 dst_sel:DWORD dst_unused:UNUSED_PAD src0_sel:WORD_1
	v_cvt_f32_f16_e32 v98, v18
	v_cvt_f32_f16_sdwa v99, v18 dst_sel:DWORD dst_unused:UNUSED_PAD src0_sel:WORD_1
	v_cvt_f32_f16_e32 v24, v20
	v_cvt_f32_f16_sdwa v25, v20 dst_sel:DWORD dst_unused:UNUSED_PAD src0_sel:WORD_1
	s_waitcnt vmcnt(1)
	v_cvt_f32_f16_e32 v100, v10
	v_cvt_f32_f16_sdwa v101, v10 dst_sel:DWORD dst_unused:UNUSED_PAD src0_sel:WORD_1
	v_cvt_f32_f16_e32 v20, v12
	v_cvt_f32_f16_sdwa v21, v12 dst_sel:DWORD dst_unused:UNUSED_PAD src0_sel:WORD_1
	v_fma_mix_f32 v30, v44, v31, v34 op_sel_hi:[0,1,0]
	v_fma_mix_f32 v31, v44, v31, v35 op_sel:[0,1,0] op_sel_hi:[0,1,0]
	v_pk_fma_f32 v[34:35], v[44:45], v[104:105], v[36:37] op_sel_hi:[0,1,1]
	v_cvt_f32_f16_e32 v119, v13
	v_cvt_f32_f16_sdwa v13, v13 dst_sel:DWORD dst_unused:UNUSED_PAD src0_sel:WORD_1
	s_waitcnt vmcnt(0)
	v_cvt_f32_f16_sdwa v12, v17 dst_sel:DWORD dst_unused:UNUSED_PAD src0_sel:WORD_1
	v_pk_mul_f32 v[84:85], v[84:85], v[88:89]
	v_fma_mix_f32 v26, v60, v27, v30 op_sel_hi:[0,1,0]
	v_fma_mix_f32 v27, v60, v27, v31 op_sel:[0,1,0] op_sel_hi:[0,1,0]
	v_pk_fma_f32 v[30:31], v[60:61], v[32:33], v[34:35] op_sel_hi:[0,1,1]
	v_cvt_f32_f16_e32 v106, v16
	v_cvt_f32_f16_sdwa v107, v16 dst_sel:DWORD dst_unused:UNUSED_PAD src0_sel:WORD_1
	v_cvt_f32_f16_e32 v120, v17
	v_mul_f32_e32 v16, v44, v49
	v_fma_mix_f32 v22, v42, v23, v26 op_sel_hi:[0,1,0]
	v_fma_mix_f32 v23, v42, v23, v27 op_sel:[0,1,0] op_sel_hi:[0,1,0]
	v_pk_fma_f32 v[26:27], v[42:43], v[28:29], v[30:31] op_sel_hi:[0,1,1]
	v_mov_b32_e32 v17, v85
	v_mul_f32_e32 v116, v45, v53
	v_mul_f32_e32 v118, v43, v117
	v_pk_mul_f32 v[82:83], v[82:83], v[90:91]
	v_pk_fma_f32 v[38:39], v[44:45], v[92:93], v[38:39] op_sel_hi:[0,1,1]
	v_fma_mix_f32 v18, v86, v19, v22 op_sel_hi:[0,1,0]
	v_fma_mix_f32 v19, v86, v19, v23 op_sel:[0,1,0] op_sel_hi:[0,1,0]
	v_pk_fma_f32 v[22:23], v[86:87], v[24:25], v[26:27] op_sel_hi:[0,1,1]
	v_pk_add_f32 v[16:17], v[40:41], v[16:17]
	v_mov_b32_e32 v117, v84
	v_mul_f32_e32 v88, v42, v87
	v_pk_fma_f32 v[36:37], v[60:61], v[94:95], v[38:39] op_sel_hi:[0,1,1]
	v_fma_mix_f32 v10, v46, v11, v18 op_sel_hi:[0,1,0]
	v_fma_mix_f32 v11, v46, v11, v19 op_sel:[0,1,0] op_sel_hi:[0,1,0]
	v_pk_fma_f32 v[18:19], v[46:47], v[20:21], v[22:23] op_sel_hi:[0,1,1]
	v_mov_b32_e32 v22, v47
	v_mov_b32_e32 v23, v46
	v_pk_add_f32 v[16:17], v[116:117], v[16:17]
	v_mov_b32_e32 v89, v83
	v_mul_f32_e32 v90, v46, v119
	v_pk_fma_f32 v[32:33], v[42:43], v[96:97], v[36:37] op_sel_hi:[0,1,1]
	v_pk_mul_f32 v[12:13], v[22:23], v[12:13]
	v_pk_add_f32 v[16:17], v[88:89], v[16:17]
	v_mov_b32_e32 v119, v82
	v_pk_fma_f32 v[28:29], v[86:87], v[98:99], v[32:33] op_sel_hi:[0,1,1]
	v_pk_add_f32 v[16:17], v[118:119], v[16:17]
	v_mov_b32_e32 v91, v13
	v_pk_fma_f32 v[24:25], v[46:47], v[100:101], v[28:29] op_sel_hi:[0,1,1]
	v_mul_f32_e32 v20, v47, v120
	v_pk_add_f32 v[16:17], v[90:91], v[16:17]
	v_mov_b32_e32 v21, v12
	v_fma_mix_f32 v38, v48, v14, v24 op_sel_hi:[0,1,0]
	v_fma_mix_f32 v39, v48, v14, v25 op_sel:[0,1,0] op_sel_hi:[0,1,0]
	v_fma_mix_f32 v34, v48, v15, v10 op_sel_hi:[0,1,0]
	v_fma_mix_f32 v35, v48, v15, v11 op_sel:[0,1,0] op_sel_hi:[0,1,0]
	v_pk_fma_f32 v[36:37], v[48:49], v[106:107], v[18:19] op_sel_hi:[0,1,1]
	v_pk_add_f32 v[40:41], v[20:21], v[16:17]

.LBB2_14:
	s_or_b64 exec, exec, s[10:11]
	s_waitcnt lgkmcnt(7)
	ds_read2_b32 v[10:11], v51 offset0:64 offset1:68
	s_waitcnt lgkmcnt(7)
	ds_read2_b32 v[12:13], v51 offset0:72 offset1:76
	s_waitcnt lgkmcnt(7)
	ds_read2_b32 v[14:15], v51 offset0:96 offset1:100
	s_waitcnt lgkmcnt(2)
	v_lshl_add_u32 v10, v10, 7, v110
	global_load_dwordx4 v[46:49], v10, s[34:35]
	v_lshl_add_u32 v10, v11, 7, v110
	global_load_dwordx4 v[42:45], v10, s[34:35]
	s_waitcnt lgkmcnt(1)
	v_lshl_add_u32 v10, v12, 7, v110
	global_load_dwordx4 v[34:37], v10, s[34:35]
	v_lshl_add_u32 v10, v13, 7, v110
	global_load_dwordx4 v[38:41], v10, s[34:35]
	ds_read2_b32 v[10:11], v51 offset0:80 offset1:84
	s_waitcnt lgkmcnt(0)
	v_lshl_add_u32 v10, v10, 7, v110
	global_load_dwordx4 v[26:29], v10, s[34:35]
	v_lshl_add_u32 v10, v11, 7, v110
	global_load_dwordx4 v[30:33], v10, s[34:35]
	ds_read2_b32 v[10:11], v51 offset0:88 offset1:92
	s_waitcnt lgkmcnt(0)
	v_lshl_add_u32 v10, v10, 7, v110
	global_load_dwordx4 v[22:25], v10, s[34:35]
	v_lshl_add_u32 v10, v11, 7, v110
	global_load_dwordx4 v[18:21], v10, s[34:35]
	v_lshl_add_u32 v10, v14, 7, v110
	global_load_dwordx4 v[10:13], v10, s[34:35]
	v_lshl_add_u32 v14, v15, 7, v110
	global_load_dwordx4 v[14:17], v14, s[34:35]
	ds_read2_b32 v[104:105], v114 offset0:64 offset1:68
	ds_read2_b32 v[102:103], v114 offset0:72 offset1:76
	s_waitcnt lgkmcnt(1)
	v_mov_b32_e32 v90, v105
	s_waitcnt lgkmcnt(0)
	v_mov_b32_e32 v100, v103
	v_mov_b32_e32 v101, v102
	v_mov_b32_e32 v91, v104
	s_waitcnt vmcnt(9)
	s_waitcnt vmcnt(7)
	v_cvt_f32_f16_sdwa v95, v37 dst_sel:DWORD dst_unused:UNUSED_PAD src0_sel:WORD_1
	v_fma_mix_f32 v106, v104, v46, v106 op_sel_hi:[0,1,0]
	v_fma_mix_f32 v107, v104, v46, v107 op_sel:[0,1,0] op_sel_hi:[0,1,0]
	v_cvt_f32_f16_e32 v116, v42
	v_cvt_f32_f16_sdwa v117, v42 dst_sel:DWORD dst_unused:UNUSED_PAD src0_sel:WORD_1
	v_mov_b32_e32 v42, v105
	v_fma_mix_f32 v46, v104, v47, v98 op_sel_hi:[0,1,0]
	v_fma_mix_f32 v47, v104, v47, v99 op_sel:[0,1,0] op_sel_hi:[0,1,0]
	v_pk_fma_f32 v[106:107], v[42:43], v[116:117], v[106:107] op_sel_hi:[0,1,1]
	v_cvt_f32_f16_e32 v116, v34
	v_cvt_f32_f16_sdwa v117, v34 dst_sel:DWORD dst_unused:UNUSED_PAD src0_sel:WORD_1
	s_waitcnt vmcnt(6)
	v_cvt_f32_f16_sdwa v94, v41 dst_sel:DWORD dst_unused:UNUSED_PAD src0_sel:WORD_1
	v_mov_b32_e32 v34, v103
	v_pk_fma_f32 v[106:107], v[102:103], v[116:117], v[106:107] op_sel_hi:[0,1,1]
	v_fma_mix_f32 v46, v42, v43, v46 op_sel_hi:[0,1,0]
	v_fma_mix_f32 v47, v42, v43, v47 op_sel:[0,1,0] op_sel_hi:[0,1,0]
	v_pk_mul_f32 v[94:95], v[100:101], v[94:95]
	ds_read2_b32 v[100:101], v114 offset0:80 offset1:84
	v_fma_mix_f32 v106, v34, v38, v106 op_sel_hi:[0,1,0]
	v_fma_mix_f32 v107, v34, v38, v107 op_sel:[0,1,0] op_sel_hi:[0,1,0]
	s_waitcnt vmcnt(5)
	v_cvt_f32_f16_e32 v116, v26
	v_cvt_f32_f16_sdwa v117, v26 dst_sel:DWORD dst_unused:UNUSED_PAD src0_sel:WORD_1
	v_fma_mix_f32 v46, v102, v35, v46 op_sel_hi:[0,1,0]
	v_fma_mix_f32 v47, v102, v35, v47 op_sel:[0,1,0] op_sel_hi:[0,1,0]
	v_fma_mix_f32 v38, v34, v39, v46 op_sel_hi:[0,1,0]
	v_fma_mix_f32 v39, v34, v39, v47 op_sel:[0,1,0] op_sel_hi:[0,1,0]
	s_waitcnt lgkmcnt(0)
	v_fma_mix_f32 v26, v100, v27, v38 op_sel_hi:[0,1,0]
	v_fma_mix_f32 v27, v100, v27, v39 op_sel:[0,1,0] op_sel_hi:[0,1,0]
	v_cvt_f32_f16_e32 v60, v49
	v_cvt_f32_f16_sdwa v86, v45 dst_sel:DWORD dst_unused:UNUSED_PAD src0_sel:WORD_1
	v_fma_mix_f32 v38, v104, v48, v96 op_sel_hi:[0,1,0]
	v_fma_mix_f32 v39, v104, v48, v97 op_sel:[0,1,0] op_sel_hi:[0,1,0]
	v_fma_mix_f32 v38, v42, v44, v38 op_sel_hi:[0,1,0]
	v_fma_mix_f32 v39, v42, v44, v39 op_sel:[0,1,0] op_sel_hi:[0,1,0]
	v_mul_f32_e32 v88, v104, v60
	v_cvt_f32_f16_e32 v60, v45
	v_cvt_f32_f16_e32 v45, v37
	v_fma_mix_f32 v37, v102, v36, v39 op_sel:[0,1,0] op_sel_hi:[0,1,0]
	v_fma_mix_f32 v36, v102, v36, v38 op_sel_hi:[0,1,0]
	v_cvt_f32_f16_sdwa v87, v49 dst_sel:DWORD dst_unused:UNUSED_PAD src0_sel:WORD_1
	s_waitcnt vmcnt(4)
	v_cvt_f32_f16_e32 v96, v30
	v_cvt_f32_f16_sdwa v97, v30 dst_sel:DWORD dst_unused:UNUSED_PAD src0_sel:WORD_1
	v_fma_mix_f32 v35, v34, v40, v37 op_sel:[0,1,0] op_sel_hi:[0,1,0]
	v_fma_mix_f32 v34, v34, v40, v36 op_sel_hi:[0,1,0]
	v_cvt_f32_f16_e32 v36, v28
	v_cvt_f32_f16_sdwa v37, v28 dst_sel:DWORD dst_unused:UNUSED_PAD src0_sel:WORD_1
	v_cvt_f32_f16_e32 v28, v29
	v_cvt_f32_f16_sdwa v30, v33 dst_sel:DWORD dst_unused:UNUSED_PAD src0_sel:WORD_1
	v_pk_mul_f32 v[92:93], v[90:91], v[86:87]
	v_pk_fma_f32 v[38:39], v[100:101], v[36:37], v[34:35] op_sel_hi:[0,1,1]
	v_cvt_f32_f16_e32 v36, v31
	v_cvt_f32_f16_sdwa v37, v31 dst_sel:DWORD dst_unused:UNUSED_PAD src0_sel:WORD_1
	v_cvt_f32_f16_sdwa v31, v29 dst_sel:DWORD dst_unused:UNUSED_PAD src0_sel:WORD_1
	v_mul_f32_e32 v90, v102, v45
	v_cvt_f32_f16_e32 v45, v41
	v_mul_f32_e32 v34, v100, v28
	v_cvt_f32_f16_e32 v42, v32
	v_cvt_f32_f16_sdwa v43, v32 dst_sel:DWORD dst_unused:UNUSED_PAD src0_sel:WORD_1
	v_cvt_f32_f16_e32 v28, v33
	v_mov_b32_e32 v32, v101
	v_mov_b32_e32 v33, v100
	v_mov_b32_e32 v89, v93
	v_mul_f32_e32 v84, v105, v60
	v_pk_mul_f32 v[30:31], v[32:33], v[30:31]
	v_pk_add_f32 v[32:33], v[82:83], v[88:89]
	v_mov_b32_e32 v85, v92
	v_pk_add_f32 v[32:33], v[84:85], v[32:33]
	v_mov_b32_e32 v91, v95
	v_mul_f32_e32 v86, v103, v45
	v_pk_add_f32 v[32:33], v[90:91], v[32:33]
	v_mov_b32_e32 v87, v94
	v_pk_add_f32 v[32:33], v[86:87], v[32:33]
	v_mov_b32_e32 v35, v31
	ds_read2_b32 v[46:47], v114 offset0:88 offset1:92
	v_pk_add_f32 v[32:33], v[34:35], v[32:33]
	s_waitcnt vmcnt(3)
	v_pk_fma_f32 v[106:107], v[100:101], v[116:117], v[106:107] op_sel_hi:[0,1,1]
	v_mov_b32_e32 v40, v101
	v_pk_fma_f32 v[88:89], v[40:41], v[96:97], v[106:107] op_sel_hi:[0,1,1]
	s_waitcnt lgkmcnt(0)
	v_fma_mix_f32 v34, v46, v22, v88 op_sel_hi:[0,1,0]
	v_fma_mix_f32 v35, v46, v22, v89 op_sel:[0,1,0] op_sel_hi:[0,1,0]
	s_waitcnt vmcnt(2)
	v_cvt_f32_f16_e32 v88, v18
	v_cvt_f32_f16_sdwa v89, v18 dst_sel:DWORD dst_unused:UNUSED_PAD src0_sel:WORD_1
	ds_read2_b32 v[82:83], v114 offset0:96 offset1:100
	v_mov_b32_e32 v18, v47
	v_pk_fma_f32 v[26:27], v[40:41], v[36:37], v[26:27] op_sel_hi:[0,1,1]
	v_pk_fma_f32 v[34:35], v[18:19], v[88:89], v[34:35] op_sel_hi:[0,1,1]
	s_waitcnt vmcnt(1)
	v_fma_mix_f32 v26, v46, v23, v26 op_sel_hi:[0,1,0]
	v_fma_mix_f32 v27, v46, v23, v27 op_sel:[0,1,0] op_sel_hi:[0,1,0]
	v_fma_mix_f32 v26, v18, v19, v26 op_sel_hi:[0,1,0]
	v_fma_mix_f32 v27, v18, v19, v27 op_sel:[0,1,0] op_sel_hi:[0,1,0]
	s_waitcnt lgkmcnt(0)
	v_fma_mix_f32 v34, v82, v10, v34 op_sel_hi:[0,1,0]
	v_fma_mix_f32 v35, v82, v10, v35 op_sel:[0,1,0] op_sel_hi:[0,1,0]
	s_waitcnt vmcnt(0)
	v_cvt_f32_f16_e32 v88, v14
	v_cvt_f32_f16_sdwa v89, v14 dst_sel:DWORD dst_unused:UNUSED_PAD src0_sel:WORD_1
	v_mov_b32_e32 v10, v83
	v_fma_mix_f32 v26, v82, v11, v26 op_sel_hi:[0,1,0]
	v_fma_mix_f32 v27, v82, v11, v27 op_sel:[0,1,0] op_sel_hi:[0,1,0]
	v_fma_mix_f32 v36, v10, v15, v26 op_sel_hi:[0,1,0]
	v_fma_mix_f32 v37, v10, v15, v27 op_sel:[0,1,0] op_sel_hi:[0,1,0]
	v_pk_fma_f32 v[14:15], v[40:41], v[42:43], v[38:39] op_sel_hi:[0,1,1]
	v_fma_mix_f32 v14, v46, v24, v14 op_sel_hi:[0,1,0]
	v_fma_mix_f32 v15, v46, v24, v15 op_sel:[0,1,0] op_sel_hi:[0,1,0]
	v_cvt_f32_f16_sdwa v45, v25 dst_sel:DWORD dst_unused:UNUSED_PAD src0_sel:WORD_1
	v_fma_mix_f32 v14, v18, v20, v14 op_sel_hi:[0,1,0]
	v_fma_mix_f32 v15, v18, v20, v15 op_sel:[0,1,0] op_sel_hi:[0,1,0]
	v_cvt_f32_f16_sdwa v44, v21 dst_sel:DWORD dst_unused:UNUSED_PAD src0_sel:WORD_1
	v_cvt_f32_f16_e32 v22, v25
	v_cvt_f32_f16_e32 v23, v21
	v_fma_mix_f32 v14, v82, v12, v14 op_sel_hi:[0,1,0]
	v_fma_mix_f32 v15, v82, v12, v15 op_sel:[0,1,0] op_sel_hi:[0,1,0]
	v_cvt_f32_f16_e32 v21, v13
	v_cvt_f32_f16_sdwa v13, v13 dst_sel:DWORD dst_unused:UNUSED_PAD src0_sel:WORD_1
	v_cvt_f32_f16_sdwa v12, v17 dst_sel:DWORD dst_unused:UNUSED_PAD src0_sel:WORD_1
	v_mov_b32_e32 v48, v47
	v_mov_b32_e32 v49, v46
	v_mul_f32_e32 v28, v101, v28
	v_pk_mul_f32 v[44:45], v[48:49], v[44:45]
	v_pk_fma_f32 v[34:35], v[10:11], v[88:89], v[34:35] op_sel_hi:[0,1,1]
	v_fma_mix_f32 v38, v10, v16, v14 op_sel_hi:[0,1,0]
	v_fma_mix_f32 v39, v10, v16, v15 op_sel:[0,1,0] op_sel_hi:[0,1,0]
	v_cvt_f32_f16_e32 v10, v17
	v_mov_b32_e32 v14, v83
	v_mov_b32_e32 v15, v82
	v_mov_b32_e32 v29, v30
	v_mul_f32_e32 v22, v46, v22
	v_mul_f32_e32 v24, v47, v23
	v_pk_mul_f32 v[12:13], v[14:15], v[12:13]
	v_pk_add_f32 v[14:15], v[28:29], v[32:33]
	v_mov_b32_e32 v23, v45
	v_pk_add_f32 v[14:15], v[22:23], v[14:15]
	v_mov_b32_e32 v25, v44
	v_mul_f32_e32 v48, v82, v21
	v_pk_add_f32 v[14:15], v[24:25], v[14:15]
	v_mov_b32_e32 v49, v13
	v_mul_f32_e32 v10, v83, v10
	v_pk_add_f32 v[14:15], v[48:49], v[14:15]
	v_mov_b32_e32 v11, v12
	v_pk_add_f32 v[40:41], v[10:11], v[14:15]
	s_and_saveexec_b64 s[10:11], s[6:7]
	s_cbranch_execz .LBB2_16
	ds_read2_b32 v[10:11], v51 offset0:104 offset1:108
	ds_read2_b32 v[12:13], v51 offset0:112 offset1:116
	ds_read2_b32 v[14:15], v51 offset0:120 offset1:124
	s_waitcnt lgkmcnt(2)
	v_lshl_add_u32 v10, v10, 7, v110
	v_lshl_add_u32 v11, v11, 7, v110
	global_load_dwordx4 v[30:33], v10, s[34:35]
	global_load_dwordx4 v[26:29], v11, s[34:35]
	s_waitcnt lgkmcnt(1)
	v_lshl_add_u32 v10, v12, 7, v110
	v_lshl_add_u32 v11, v13, 7, v110
	global_load_dwordx4 v[22:25], v10, s[34:35]
	global_load_dwordx4 v[18:21], v11, s[34:35]
	s_waitcnt lgkmcnt(0)
	v_lshl_add_u32 v10, v14, 7, v110
	global_load_dwordx4 v[10:13], v10, s[34:35]
	v_lshl_add_u32 v14, v15, 7, v110
	global_load_dwordx4 v[14:17], v14, s[34:35]
	ds_read2_b32 v[44:45], v114 offset0:104 offset1:108
	ds_read2_b32 v[42:43], v114 offset0:112 offset1:116
	ds_read2_b32 v[46:47], v114 offset0:120 offset1:124
	s_waitcnt lgkmcnt(2)
	v_mov_b32_e32 v84, v45
	v_mov_b32_e32 v85, v44
	v_mov_b32_e32 v60, v45
	s_waitcnt lgkmcnt(1)
	v_mov_b32_e32 v82, v43
	v_mov_b32_e32 v83, v42
	v_mov_b32_e32 v86, v43
	s_waitcnt lgkmcnt(0)
	v_mov_b32_e32 v48, v47
	s_waitcnt vmcnt(5)
	v_cvt_f32_f16_e32 v92, v30
	v_cvt_f32_f16_sdwa v93, v30 dst_sel:DWORD dst_unused:UNUSED_PAD src0_sel:WORD_1
	v_cvt_f32_f16_e32 v104, v32
	v_cvt_f32_f16_sdwa v105, v32 dst_sel:DWORD dst_unused:UNUSED_PAD src0_sel:WORD_1
	v_cvt_f32_f16_e32 v49, v33
	v_cvt_f32_f16_sdwa v89, v33 dst_sel:DWORD dst_unused:UNUSED_PAD src0_sel:WORD_1
	s_waitcnt vmcnt(4)
	v_cvt_f32_f16_sdwa v88, v29 dst_sel:DWORD dst_unused:UNUSED_PAD src0_sel:WORD_1
	v_cvt_f32_f16_e32 v94, v26
	v_cvt_f32_f16_sdwa v95, v26 dst_sel:DWORD dst_unused:UNUSED_PAD src0_sel:WORD_1
	v_cvt_f32_f16_e32 v32, v28
	v_cvt_f32_f16_sdwa v33, v28 dst_sel:DWORD dst_unused:UNUSED_PAD src0_sel:WORD_1
	v_cvt_f32_f16_e32 v87, v29
	s_waitcnt vmcnt(3)
	v_cvt_f32_f16_e32 v96, v22
	v_cvt_f32_f16_sdwa v97, v22 dst_sel:DWORD dst_unused:UNUSED_PAD src0_sel:WORD_1
	v_cvt_f32_f16_e32 v28, v24
	v_cvt_f32_f16_sdwa v29, v24 dst_sel:DWORD dst_unused:UNUSED_PAD src0_sel:WORD_1
	v_cvt_f32_f16_e32 v117, v25
	v_cvt_f32_f16_sdwa v91, v25 dst_sel:DWORD dst_unused:UNUSED_PAD src0_sel:WORD_1
	s_waitcnt vmcnt(2)
	v_cvt_f32_f16_sdwa v90, v21 dst_sel:DWORD dst_unused:UNUSED_PAD src0_sel:WORD_1
	v_cvt_f32_f16_e32 v98, v18
	v_cvt_f32_f16_sdwa v99, v18 dst_sel:DWORD dst_unused:UNUSED_PAD src0_sel:WORD_1
	v_cvt_f32_f16_e32 v24, v20
	v_cvt_f32_f16_sdwa v25, v20 dst_sel:DWORD dst_unused:UNUSED_PAD src0_sel:WORD_1
	v_cvt_f32_f16_e32 v118, v21
	s_waitcnt vmcnt(1)
	v_cvt_f32_f16_e32 v100, v10
	v_cvt_f32_f16_sdwa v101, v10 dst_sel:DWORD dst_unused:UNUSED_PAD src0_sel:WORD_1
	v_cvt_f32_f16_e32 v20, v12
	v_cvt_f32_f16_sdwa v21, v12 dst_sel:DWORD dst_unused:UNUSED_PAD src0_sel:WORD_1
	v_fma_mix_f32 v30, v44, v31, v36 op_sel_hi:[0,1,0]
	v_fma_mix_f32 v31, v44, v31, v37 op_sel:[0,1,0] op_sel_hi:[0,1,0]
	v_pk_fma_f32 v[36:37], v[44:45], v[104:105], v[38:39] op_sel_hi:[0,1,1]
	v_cvt_f32_f16_e32 v119, v13
	v_cvt_f32_f16_sdwa v13, v13 dst_sel:DWORD dst_unused:UNUSED_PAD src0_sel:WORD_1
	s_waitcnt vmcnt(0)
	v_cvt_f32_f16_sdwa v12, v17 dst_sel:DWORD dst_unused:UNUSED_PAD src0_sel:WORD_1
	v_pk_mul_f32 v[84:85], v[84:85], v[88:89]
	v_fma_mix_f32 v26, v60, v27, v30 op_sel_hi:[0,1,0]
	v_fma_mix_f32 v27, v60, v27, v31 op_sel:[0,1,0] op_sel_hi:[0,1,0]
	v_pk_fma_f32 v[30:31], v[60:61], v[32:33], v[36:37] op_sel_hi:[0,1,1]
	v_cvt_f32_f16_e32 v106, v16
	v_cvt_f32_f16_sdwa v107, v16 dst_sel:DWORD dst_unused:UNUSED_PAD src0_sel:WORD_1
	v_cvt_f32_f16_e32 v120, v17
	v_mul_f32_e32 v16, v44, v49
	v_fma_mix_f32 v22, v42, v23, v26 op_sel_hi:[0,1,0]
	v_fma_mix_f32 v23, v42, v23, v27 op_sel:[0,1,0] op_sel_hi:[0,1,0]
	v_pk_fma_f32 v[26:27], v[42:43], v[28:29], v[30:31] op_sel_hi:[0,1,1]
	v_mov_b32_e32 v17, v85
	v_mul_f32_e32 v116, v45, v87
	v_mul_f32_e32 v88, v42, v117
	v_pk_mul_f32 v[82:83], v[82:83], v[90:91]
	v_pk_fma_f32 v[34:35], v[44:45], v[92:93], v[34:35] op_sel_hi:[0,1,1]
	v_fma_mix_f32 v18, v86, v19, v22 op_sel_hi:[0,1,0]
	v_fma_mix_f32 v19, v86, v19, v23 op_sel:[0,1,0] op_sel_hi:[0,1,0]
	v_pk_fma_f32 v[22:23], v[86:87], v[24:25], v[26:27] op_sel_hi:[0,1,1]
	v_pk_add_f32 v[16:17], v[40:41], v[16:17]
	v_mov_b32_e32 v117, v84
	v_pk_fma_f32 v[34:35], v[60:61], v[94:95], v[34:35] op_sel_hi:[0,1,1]
	v_fma_mix_f32 v10, v46, v11, v18 op_sel_hi:[0,1,0]
	v_fma_mix_f32 v11, v46, v11, v19 op_sel:[0,1,0] op_sel_hi:[0,1,0]
	v_pk_fma_f32 v[18:19], v[46:47], v[20:21], v[22:23] op_sel_hi:[0,1,1]
	v_mov_b32_e32 v22, v47
	v_mov_b32_e32 v23, v46
	v_pk_add_f32 v[16:17], v[116:117], v[16:17]
	v_mov_b32_e32 v89, v83
	v_mul_f32_e32 v118, v43, v118
	v_mul_f32_e32 v90, v46, v119
	v_pk_fma_f32 v[32:33], v[42:43], v[96:97], v[34:35] op_sel_hi:[0,1,1]
	v_pk_mul_f32 v[12:13], v[22:23], v[12:13]
	v_pk_add_f32 v[16:17], v[88:89], v[16:17]
	v_mov_b32_e32 v119, v82
	v_pk_fma_f32 v[28:29], v[86:87], v[98:99], v[32:33] op_sel_hi:[0,1,1]
	v_pk_add_f32 v[16:17], v[118:119], v[16:17]
	v_mov_b32_e32 v91, v13
	v_pk_fma_f32 v[24:25], v[46:47], v[100:101], v[28:29] op_sel_hi:[0,1,1]
	v_mul_f32_e32 v20, v47, v120
	v_pk_add_f32 v[16:17], v[90:91], v[16:17]
	v_mov_b32_e32 v21, v12
	v_fma_mix_f32 v34, v48, v14, v24 op_sel_hi:[0,1,0]
	v_fma_mix_f32 v35, v48, v14, v25 op_sel:[0,1,0] op_sel_hi:[0,1,0]
	v_fma_mix_f32 v36, v48, v15, v10 op_sel_hi:[0,1,0]
	v_fma_mix_f32 v37, v48, v15, v11 op_sel:[0,1,0] op_sel_hi:[0,1,0]
	v_pk_fma_f32 v[38:39], v[48:49], v[106:107], v[18:19] op_sel_hi:[0,1,1]
	v_pk_add_f32 v[40:41], v[20:21], v[16:17]

.LBB3_2:
	s_or_b64 exec, exec, s[2:3]
	v_mbcnt_lo_u32_b32 v10, -1, 0
	v_mbcnt_hi_u32_b32 v27, -1, v10
	s_waitcnt vmcnt(1)
	v_cmp_gt_i32_e64 s[2:3], v45, v41
	v_and_or_b32 v9, v27, 64, v9
	v_lshlrev_b32_e32 v47, 2, v9
	s_waitcnt vmcnt(0)
	v_cndmask_b32_e64 v8, v24, v8, s[2:3]
	ds_bpermute_b32 v10, v47, v8
	ds_bpermute_b32 v14, v47, v8 offset:16
	ds_bpermute_b32 v20, v47, v8 offset:48
	v_cndmask_b32_e64 v49, 0, 1.0, s[2:3]
	ds_bpermute_b32 v40, v47, v49
	s_waitcnt lgkmcnt(3)
	v_ashrrev_i32_e32 v11, 31, v10
	v_lshlrev_b64 v[10:11], 7, v[10:11]
	v_lshl_add_u64 v[10:11], v[30:31], 0, v[10:11]
	global_load_dwordx4 v[10:13], v[10:11], off
	s_waitcnt lgkmcnt(2)
	v_ashrrev_i32_e32 v15, 31, v14
	v_lshlrev_b64 v[14:15], 7, v[14:15]
	v_lshl_add_u64 v[14:15], v[30:31], 0, v[14:15]
	global_load_dwordx4 v[14:17], v[14:15], off
	s_waitcnt lgkmcnt(1)
	v_ashrrev_i32_e32 v21, 31, v20
	v_lshlrev_b64 v[22:23], 7, v[20:21]
	v_lshl_add_u64 v[22:23], v[30:31], 0, v[22:23]
	global_load_dwordx4 v[32:35], v[22:23], off
	ds_bpermute_b32 v18, v47, v8 offset:32
	ds_bpermute_b32 v42, v47, v49 offset:16
	ds_bpermute_b32 v44, v47, v49 offset:64
	v_cmp_lt_i32_e64 s[2:3], 32, v45
	s_waitcnt lgkmcnt(2)
	v_ashrrev_i32_e32 v19, 31, v18
	v_lshlrev_b64 v[18:19], 7, v[18:19]
	v_lshl_add_u64 v[18:19], v[30:31], 0, v[18:19]
	global_load_dwordx4 v[18:21], v[18:19], off
	s_waitcnt vmcnt(3)
	v_fma_mix_f32 v6, v40, v10, v6 op_sel_hi:[0,1,0]
	v_fma_mix_f32 v7, v40, v10, v7 op_sel:[0,1,0] op_sel_hi:[0,1,0]
	ds_bpermute_b32 v22, v47, v8 offset:64
	v_fma_mix_f32 v10, v40, v11, v4 op_sel_hi:[0,1,0]
	v_fma_mix_f32 v11, v40, v11, v5 op_sel:[0,1,0] op_sel_hi:[0,1,0]
	ds_bpermute_b32 v4, v47, v8 offset:80
	s_waitcnt lgkmcnt(1)
	v_ashrrev_i32_e32 v23, 31, v22
	v_fma_mix_f32 v36, v40, v12, v2 op_sel_hi:[0,1,0]
	v_fma_mix_f32 v37, v40, v12, v3 op_sel:[0,1,0] op_sel_hi:[0,1,0]
	v_lshlrev_b64 v[2:3], 7, v[22:23]
	v_lshl_add_u64 v[2:3], v[30:31], 0, v[2:3]
	s_waitcnt vmcnt(2)
	v_fma_mix_f32 v22, v40, v13, v0 op_sel_hi:[0,1,0]
	v_fma_mix_f32 v23, v40, v13, v1 op_sel:[0,1,0] op_sel_hi:[0,1,0]
	global_load_dwordx4 v[0:3], v[2:3], off
	ds_bpermute_b32 v12, v47, v8 offset:96
	s_waitcnt lgkmcnt(1)
	v_ashrrev_i32_e32 v5, 31, v4
	v_lshlrev_b64 v[4:5], 7, v[4:5]
	v_lshl_add_u64 v[4:5], v[30:31], 0, v[4:5]
	v_fma_mix_f32 v38, v42, v14, v6 op_sel_hi:[0,1,0]
	v_fma_mix_f32 v39, v42, v14, v7 op_sel:[0,1,0] op_sel_hi:[0,1,0]
	global_load_dwordx4 v[4:7], v[4:5], off
	s_waitcnt lgkmcnt(0)
	v_ashrrev_i32_e32 v13, 31, v12
	v_lshlrev_b64 v[12:13], 7, v[12:13]
	v_lshl_add_u64 v[12:13], v[30:31], 0, v[12:13]
	v_fma_mix_f32 v60, v42, v15, v10 op_sel_hi:[0,1,0]
	v_fma_mix_f32 v61, v42, v15, v11 op_sel:[0,1,0] op_sel_hi:[0,1,0]
	global_load_dwordx4 v[10:13], v[12:13], off
	ds_bpermute_b32 v40, v47, v49 offset:32
	s_waitcnt vmcnt(3)
	v_fma_mix_f32 v50, v42, v16, v36 op_sel_hi:[0,1,0]
	v_fma_mix_f32 v51, v42, v16, v37 op_sel:[0,1,0] op_sel_hi:[0,1,0]
	v_fma_mix_f32 v22, v42, v17, v22 op_sel_hi:[0,1,0]
	v_fma_mix_f32 v23, v42, v17, v23 op_sel:[0,1,0] op_sel_hi:[0,1,0]
	ds_bpermute_b32 v42, v47, v49 offset:48
	s_waitcnt lgkmcnt(1)
	v_fma_mix_f32 v14, v40, v18, v38 op_sel_hi:[0,1,0]
	v_fma_mix_f32 v15, v40, v18, v39 op_sel:[0,1,0] op_sel_hi:[0,1,0]
	s_waitcnt lgkmcnt(0)
	v_fma_mix_f32 v14, v42, v32, v14 op_sel_hi:[0,1,0]
	v_fma_mix_f32 v15, v42, v32, v15 op_sel:[0,1,0] op_sel_hi:[0,1,0]
	v_fma_mix_f32 v18, v40, v19, v60 op_sel_hi:[0,1,0]
	v_fma_mix_f32 v19, v40, v19, v61 op_sel:[0,1,0] op_sel_hi:[0,1,0]
	v_fma_mix_f32 v18, v42, v33, v18 op_sel_hi:[0,1,0]
	v_fma_mix_f32 v19, v42, v33, v19 op_sel:[0,1,0] op_sel_hi:[0,1,0]
	s_waitcnt vmcnt(2)
	v_cvt_f32_f16_e32 v16, v0
	v_cvt_f32_f16_sdwa v17, v0 dst_sel:DWORD dst_unused:UNUSED_PAD src0_sel:WORD_1
	ds_bpermute_b32 v0, v47, v49 offset:80
	v_pk_fma_f32 v[14:15], v[44:45], v[16:17], v[14:15] op_sel_hi:[0,1,1]
	s_waitcnt vmcnt(1)
	v_cvt_f32_f16_e32 v16, v4
	v_cvt_f32_f16_sdwa v17, v4 dst_sel:DWORD dst_unused:UNUSED_PAD src0_sel:WORD_1
	ds_bpermute_b32 v4, v47, v49 offset:96
	v_fma_mix_f32 v18, v44, v1, v18 op_sel_hi:[0,1,0]
	v_fma_mix_f32 v19, v44, v1, v19 op_sel:[0,1,0] op_sel_hi:[0,1,0]
	s_waitcnt lgkmcnt(1)
	v_pk_fma_f32 v[14:15], v[0:1], v[16:17], v[14:15] op_sel_hi:[0,1,1]
	s_waitcnt vmcnt(0)
	v_cvt_f32_f16_e32 v16, v10
	v_cvt_f32_f16_sdwa v17, v10 dst_sel:DWORD dst_unused:UNUSED_PAD src0_sel:WORD_1
	ds_bpermute_b32 v10, v47, v49 offset:112
	s_waitcnt lgkmcnt(1)
	v_pk_fma_f32 v[36:37], v[4:5], v[16:17], v[14:15] op_sel_hi:[0,1,1]
	ds_bpermute_b32 v14, v47, v8 offset:112
	v_fma_mix_f32 v18, v0, v5, v18 op_sel_hi:[0,1,0]
	v_fma_mix_f32 v19, v0, v5, v19 op_sel:[0,1,0] op_sel_hi:[0,1,0]
	s_waitcnt lgkmcnt(0)
	v_ashrrev_i32_e32 v15, 31, v14
	v_lshlrev_b64 v[14:15], 7, v[14:15]
	v_lshl_add_u64 v[14:15], v[30:31], 0, v[14:15]
	global_load_dwordx4 v[14:17], v[14:15], off
	v_fma_mix_f32 v18, v4, v11, v18 op_sel_hi:[0,1,0]
	v_fma_mix_f32 v19, v4, v11, v19 op_sel:[0,1,0] op_sel_hi:[0,1,0]
	s_waitcnt vmcnt(0)
	v_fma_mix_f32 v36, v10, v14, v36 op_sel_hi:[0,1,0]
	v_fma_mix_f32 v37, v10, v14, v37 op_sel:[0,1,0] op_sel_hi:[0,1,0]
	v_fma_mix_f32 v38, v10, v15, v18 op_sel_hi:[0,1,0]
	v_fma_mix_f32 v39, v10, v15, v19 op_sel:[0,1,0] op_sel_hi:[0,1,0]
	v_cvt_f32_f16_e32 v18, v2
	v_cvt_f32_f16_sdwa v19, v2 dst_sel:DWORD dst_unused:UNUSED_PAD src0_sel:WORD_1
	v_fma_mix_f32 v14, v40, v20, v50 op_sel_hi:[0,1,0]
	v_fma_mix_f32 v15, v40, v20, v51 op_sel:[0,1,0] op_sel_hi:[0,1,0]
	v_fma_mix_f32 v14, v42, v34, v14 op_sel_hi:[0,1,0]
	v_fma_mix_f32 v15, v42, v34, v15 op_sel:[0,1,0] op_sel_hi:[0,1,0]
	v_cvt_f32_f16_e32 v2, v3
	v_pk_fma_f32 v[14:15], v[44:45], v[18:19], v[14:15] op_sel_hi:[0,1,1]
	v_cvt_f32_f16_e32 v18, v6
	v_cvt_f32_f16_sdwa v19, v6 dst_sel:DWORD dst_unused:UNUSED_PAD src0_sel:WORD_1
	v_cvt_f32_f16_sdwa v3, v3 dst_sel:DWORD dst_unused:UNUSED_PAD src0_sel:WORD_1
	v_cvt_f32_f16_e32 v6, v7
	v_cvt_f32_f16_sdwa v7, v7 dst_sel:DWORD dst_unused:UNUSED_PAD src0_sel:WORD_1
	v_pk_fma_f32 v[14:15], v[0:1], v[18:19], v[14:15] op_sel_hi:[0,1,1]
	v_cvt_f32_f16_e32 v18, v12
	v_cvt_f32_f16_sdwa v19, v12 dst_sel:DWORD dst_unused:UNUSED_PAD src0_sel:WORD_1
	v_cvt_f32_f16_e32 v12, v13
	v_cvt_f32_f16_sdwa v13, v13 dst_sel:DWORD dst_unused:UNUSED_PAD src0_sel:WORD_1
	v_pk_fma_f32 v[14:15], v[4:5], v[18:19], v[14:15] op_sel_hi:[0,1,1]
	v_cvt_f32_f16_e32 v18, v16
	v_cvt_f32_f16_sdwa v19, v16 dst_sel:DWORD dst_unused:UNUSED_PAD src0_sel:WORD_1
	v_cvt_f32_f16_e32 v16, v17
	v_cvt_f32_f16_sdwa v17, v17 dst_sel:DWORD dst_unused:UNUSED_PAD src0_sel:WORD_1
	v_pk_fma_f32 v[32:33], v[10:11], v[18:19], v[14:15] op_sel_hi:[0,1,1]
	v_fma_mix_f32 v14, v40, v21, v22 op_sel_hi:[0,1,0]
	v_fma_mix_f32 v15, v40, v21, v23 op_sel:[0,1,0] op_sel_hi:[0,1,0]
	v_fma_mix_f32 v14, v42, v35, v14 op_sel_hi:[0,1,0]
	v_fma_mix_f32 v15, v42, v35, v15 op_sel:[0,1,0] op_sel_hi:[0,1,0]
	v_pk_fma_f32 v[2:3], v[44:45], v[2:3], v[14:15] op_sel_hi:[0,1,1]
	v_pk_fma_f32 v[0:1], v[0:1], v[6:7], v[2:3] op_sel_hi:[0,1,1]
	v_pk_fma_f32 v[0:1], v[4:5], v[12:13], v[0:1] op_sel_hi:[0,1,1]
	v_pk_fma_f32 v[34:35], v[10:11], v[16:17], v[0:1] op_sel_hi:[0,1,1]
	s_and_saveexec_b64 s[6:7], s[2:3]
	s_cbranch_execz .LBB3_4
	ds_bpermute_b32 v0, v47, v8 offset:128
	ds_bpermute_b32 v2, v47, v8 offset:144
	ds_bpermute_b32 v4, v47, v8 offset:176
	ds_bpermute_b32 v6, v47, v8 offset:208
	ds_bpermute_b32 v10, v47, v8 offset:224
	s_waitcnt lgkmcnt(4)
	v_ashrrev_i32_e32 v1, 31, v0
	s_waitcnt lgkmcnt(3)
	v_ashrrev_i32_e32 v3, 31, v2
	v_lshlrev_b64 v[0:1], 7, v[0:1]
	v_lshlrev_b64 v[2:3], 7, v[2:3]
	v_lshl_add_u64 v[0:1], v[30:31], 0, v[0:1]
	v_lshl_add_u64 v[2:3], v[30:31], 0, v[2:3]
	global_load_dwordx4 v[52:55], v[0:1], off
	global_load_dwordx4 v[58:61], v[2:3], off
	ds_bpermute_b32 v0, v47, v8 offset:160
	ds_bpermute_b32 v2, v47, v8 offset:192
	s_waitcnt lgkmcnt(4)
	v_ashrrev_i32_e32 v5, 31, v4
	s_waitcnt lgkmcnt(3)
	v_ashrrev_i32_e32 v7, 31, v6
	s_waitcnt lgkmcnt(2)
	v_ashrrev_i32_e32 v11, 31, v10
	s_waitcnt lgkmcnt(1)
	v_ashrrev_i32_e32 v1, 31, v0
	v_lshlrev_b64 v[0:1], 7, v[0:1]
	v_lshl_add_u64 v[0:1], v[30:31], 0, v[0:1]
	global_load_dwordx4 v[16:19], v[0:1], off
	v_lshlrev_b64 v[0:1], 7, v[4:5]
	s_waitcnt lgkmcnt(0)
	v_ashrrev_i32_e32 v3, 31, v2
	v_lshl_add_u64 v[0:1], v[30:31], 0, v[0:1]
	global_load_dwordx4 v[20:23], v[0:1], off
	v_lshlrev_b64 v[0:1], 7, v[2:3]
	v_lshl_add_u64 v[0:1], v[30:31], 0, v[0:1]
	global_load_dwordx4 v[12:15], v[0:1], off
	v_lshlrev_b64 v[0:1], 7, v[6:7]
	v_lshl_add_u64 v[0:1], v[30:31], 0, v[0:1]
	global_load_dwordx4 v[4:7], v[0:1], off
	ds_bpermute_b32 v0, v47, v8 offset:240
	v_lshlrev_b64 v[2:3], 7, v[10:11]
	v_lshl_add_u64 v[2:3], v[30:31], 0, v[2:3]
	global_load_dwordx4 v[8:11], v[2:3], off
	ds_bpermute_b32 v46, v47, v49 offset:128
	s_waitcnt lgkmcnt(1)
	v_ashrrev_i32_e32 v1, 31, v0
	v_lshlrev_b64 v[0:1], 7, v[0:1]
	v_lshl_add_u64 v[0:1], v[30:31], 0, v[0:1]
	global_load_dwordx4 v[0:3], v[0:1], off
	ds_bpermute_b32 v48, v47, v49 offset:144
	ds_bpermute_b32 v50, v47, v49 offset:160
	ds_bpermute_b32 v44, v47, v49 offset:176
	ds_bpermute_b32 v40, v47, v49 offset:192
	ds_bpermute_b32 v42, v47, v49 offset:208
	s_waitcnt vmcnt(7)
	s_waitcnt vmcnt(6)
	s_waitcnt vmcnt(5)
	s_waitcnt lgkmcnt(5)
	v_fma_mix_f32 v36, v46, v52, v36 op_sel_hi:[0,1,0]
	v_fma_mix_f32 v37, v46, v52, v37 op_sel:[0,1,0] op_sel_hi:[0,1,0]
	s_waitcnt vmcnt(4)
	v_fma_mix_f32 v38, v46, v53, v38 op_sel_hi:[0,1,0]
	v_fma_mix_f32 v39, v46, v53, v39 op_sel:[0,1,0] op_sel_hi:[0,1,0]
	s_waitcnt vmcnt(3)
	v_cvt_f32_f16_e32 v66, v54
	v_cvt_f32_f16_sdwa v67, v54 dst_sel:DWORD dst_unused:UNUSED_PAD src0_sel:WORD_1
	ds_bpermute_b32 v54, v47, v49 offset:224
	s_waitcnt lgkmcnt(5)
	v_fma_mix_f32 v36, v48, v58, v36 op_sel_hi:[0,1,0]
	v_fma_mix_f32 v37, v48, v58, v37 op_sel:[0,1,0] op_sel_hi:[0,1,0]
	s_waitcnt vmcnt(2)
	v_fma_mix_f32 v38, v48, v59, v38 op_sel_hi:[0,1,0]
	v_fma_mix_f32 v39, v48, v59, v39 op_sel:[0,1,0] op_sel_hi:[0,1,0]
	ds_bpermute_b32 v52, v47, v49 offset:240
	s_waitcnt lgkmcnt(5)
	v_fma_mix_f32 v36, v50, v16, v36 op_sel_hi:[0,1,0]
	v_fma_mix_f32 v37, v50, v16, v37 op_sel:[0,1,0] op_sel_hi:[0,1,0]
	s_waitcnt vmcnt(1)
	v_fma_mix_f32 v16, v50, v17, v38 op_sel_hi:[0,1,0]
	v_fma_mix_f32 v17, v50, v17, v39 op_sel:[0,1,0] op_sel_hi:[0,1,0]
	s_waitcnt lgkmcnt(4)
	v_fma_mix_f32 v36, v44, v20, v36 op_sel_hi:[0,1,0]
	v_fma_mix_f32 v37, v44, v20, v37 op_sel:[0,1,0] op_sel_hi:[0,1,0]
	s_waitcnt vmcnt(0)
	v_fma_mix_f32 v16, v44, v21, v16 op_sel_hi:[0,1,0]
	v_fma_mix_f32 v17, v44, v21, v17 op_sel:[0,1,0] op_sel_hi:[0,1,0]
	s_waitcnt lgkmcnt(3)
	v_fma_mix_f32 v20, v40, v12, v36 op_sel_hi:[0,1,0]
	v_fma_mix_f32 v21, v40, v12, v37 op_sel:[0,1,0] op_sel_hi:[0,1,0]
	v_fma_mix_f32 v12, v40, v13, v16 op_sel_hi:[0,1,0]
	v_fma_mix_f32 v13, v40, v13, v17 op_sel:[0,1,0] op_sel_hi:[0,1,0]
	s_waitcnt lgkmcnt(2)
	v_fma_mix_f32 v20, v42, v4, v20 op_sel_hi:[0,1,0]
	v_fma_mix_f32 v21, v42, v4, v21 op_sel:[0,1,0] op_sel_hi:[0,1,0]
	v_fma_mix_f32 v4, v42, v5, v12 op_sel_hi:[0,1,0]
	v_fma_mix_f32 v5, v42, v5, v13 op_sel:[0,1,0] op_sel_hi:[0,1,0]
	s_waitcnt lgkmcnt(1)
	v_fma_mix_f32 v20, v54, v8, v20 op_sel_hi:[0,1,0]
	v_fma_mix_f32 v21, v54, v8, v21 op_sel:[0,1,0] op_sel_hi:[0,1,0]
	v_fma_mix_f32 v4, v54, v9, v4 op_sel_hi:[0,1,0]
	v_fma_mix_f32 v5, v54, v9, v5 op_sel:[0,1,0] op_sel_hi:[0,1,0]
	s_waitcnt lgkmcnt(0)
	v_fma_mix_f32 v36, v52, v0, v20 op_sel_hi:[0,1,0]
	v_fma_mix_f32 v37, v52, v0, v21 op_sel:[0,1,0] op_sel_hi:[0,1,0]
	v_fma_mix_f32 v38, v52, v1, v4 op_sel_hi:[0,1,0]
	v_fma_mix_f32 v39, v52, v1, v5 op_sel:[0,1,0] op_sel_hi:[0,1,0]
	v_pk_fma_f32 v[8:9], v[46:47], v[66:67], v[32:33] op_sel_hi:[0,1,1]
	v_fma_mix_f32 v8, v48, v60, v8 op_sel_hi:[0,1,0]
	v_fma_mix_f32 v9, v48, v60, v9 op_sel:[0,1,0] op_sel_hi:[0,1,0]
	v_fma_mix_f32 v0, v50, v18, v8 op_sel_hi:[0,1,0]
	v_fma_mix_f32 v1, v50, v18, v9 op_sel:[0,1,0] op_sel_hi:[0,1,0]
	v_fma_mix_f32 v0, v44, v22, v0 op_sel_hi:[0,1,0]
	v_fma_mix_f32 v1, v44, v22, v1 op_sel:[0,1,0] op_sel_hi:[0,1,0]
	v_fma_mix_f32 v0, v40, v14, v0 op_sel_hi:[0,1,0]
	v_fma_mix_f32 v1, v40, v14, v1 op_sel:[0,1,0] op_sel_hi:[0,1,0]
	v_fma_mix_f32 v0, v42, v6, v0 op_sel_hi:[0,1,0]
	v_fma_mix_f32 v1, v42, v6, v1 op_sel:[0,1,0] op_sel_hi:[0,1,0]
	v_fma_mix_f32 v0, v54, v10, v0 op_sel_hi:[0,1,0]
	v_fma_mix_f32 v1, v54, v10, v1 op_sel:[0,1,0] op_sel_hi:[0,1,0]
	v_fma_mix_f32 v32, v52, v2, v0 op_sel_hi:[0,1,0]
	v_fma_mix_f32 v33, v52, v2, v1 op_sel:[0,1,0] op_sel_hi:[0,1,0]
	v_fma_mix_f32 v8, v46, v55, v34 op_sel_hi:[0,1,0]
	v_fma_mix_f32 v9, v46, v55, v35 op_sel:[0,1,0] op_sel_hi:[0,1,0]
	v_fma_mix_f32 v8, v48, v61, v8 op_sel_hi:[0,1,0]
	v_fma_mix_f32 v9, v48, v61, v9 op_sel:[0,1,0] op_sel_hi:[0,1,0]
	v_fma_mix_f32 v0, v50, v19, v8 op_sel_hi:[0,1,0]
	v_fma_mix_f32 v1, v50, v19, v9 op_sel:[0,1,0] op_sel_hi:[0,1,0]
	v_fma_mix_f32 v0, v44, v23, v0 op_sel_hi:[0,1,0]
	v_fma_mix_f32 v1, v44, v23, v1 op_sel:[0,1,0] op_sel_hi:[0,1,0]
	v_fma_mix_f32 v0, v40, v15, v0 op_sel_hi:[0,1,0]
	v_fma_mix_f32 v1, v40, v15, v1 op_sel:[0,1,0] op_sel_hi:[0,1,0]
	v_fma_mix_f32 v0, v42, v7, v0 op_sel_hi:[0,1,0]
	v_fma_mix_f32 v1, v42, v7, v1 op_sel:[0,1,0] op_sel_hi:[0,1,0]
	v_fma_mix_f32 v0, v54, v11, v0 op_sel_hi:[0,1,0]
	v_fma_mix_f32 v1, v54, v11, v1 op_sel:[0,1,0] op_sel_hi:[0,1,0]
	v_fma_mix_f32 v34, v52, v3, v0 op_sel_hi:[0,1,0]
	v_fma_mix_f32 v35, v52, v3, v1 op_sel:[0,1,0] op_sel_hi:[0,1,0]

.LBB4_4:
	s_or_b64 exec, exec, s[8:9]
	s_waitcnt vmcnt(0)
	s_waitcnt lgkmcnt(0)
	s_add_i32 s10, s10, 4
	v_fma_mix_f32 v6, v14, v13, v6 op_sel_hi:[0,1,0]
	v_fma_mix_f32 v7, v14, v13, v7 op_sel:[0,1,0] op_sel_hi:[0,1,0]
	v_fma_mix_f32 v4, v14, v12, v4 op_sel_hi:[0,1,0]
	v_fma_mix_f32 v5, v14, v12, v5 op_sel:[0,1,0] op_sel_hi:[0,1,0]
	v_fma_mix_f32 v2, v14, v11, v2 op_sel_hi:[0,1,0]
	v_fma_mix_f32 v3, v14, v11, v3 op_sel:[0,1,0] op_sel_hi:[0,1,0]
	v_fma_mix_f32 v0, v14, v10, v0 op_sel_hi:[0,1,0]
	v_fma_mix_f32 v1, v14, v10, v1 op_sel:[0,1,0] op_sel_hi:[0,1,0]
	s_cmp_lt_u32 s10, 60
	v_add_u32_e32 v24, 16, v24
	s_cbranch_scc0 .LBB4_7

.LBB4_13:
	s_or_b64 exec, exec, s[8:9]
	v_lshlrev_b32_e32 v58, 9, v53
	v_cmp_lt_i32_e32 vcc, v52, v57
	v_or_b32_e32 v1, 0x800, v58
	v_or_b32_e32 v2, v1, v46
	s_waitcnt vmcnt(0)
	v_cndmask_b32_e32 v0, v44, v24, vcc
	ds_write2st64_b32 v2, v0, v50 offset1:1
	v_lshlrev_b32_e32 v50, 2, v55
	v_or_b32_e32 v26, v1, v50
	ds_read2_b32 v[0:1], v26 offset1:4
	ds_read2_b32 v[20:21], v26 offset0:16 offset1:20
	v_lshl_or_b32 v45, v47, 4, v8
	v_cndmask_b32_e32 v59, 0, v25, vcc
	ds_read2_b32 v[24:25], v26 offset0:24 offset1:28
	s_waitcnt lgkmcnt(2)
	v_lshl_add_u32 v0, v0, 7, v45
	s_waitcnt lgkmcnt(1)
	v_lshl_add_u32 v16, v20, 7, v45
	global_load_dwordx4 v[8:11], v0, s[4:5]
	v_lshl_add_u32 v20, v21, 7, v45
	global_load_dwordx4 v[16:19], v16, s[4:5]
	v_lshl_add_u32 v0, v1, 7, v45
	global_load_dwordx4 v[12:15], v0, s[4:5]
	v_or_b32_e32 v27, 0x1000, v58
	global_load_dwordx4 v[20:23], v20, s[4:5]
	ds_read2_b32 v[0:1], v26 offset0:8 offset1:12
	s_waitcnt lgkmcnt(1)
	v_lshl_add_u32 v24, v24, 7, v45
	v_or_b32_e32 v30, v27, v46
	v_or_b32_e32 v60, v27, v50
	s_mov_b32 s3, 48
	s_waitcnt lgkmcnt(0)
	v_lshl_add_u32 v0, v0, 7, v45
	global_load_dwordx4 v[4:7], v0, s[4:5]
	v_lshl_add_u32 v0, v1, 7, v45
	global_load_dwordx4 v[0:3], v0, s[4:5]
	ds_read2_b32 v[28:29], v26 offset0:32 offset1:36
	ds_read2_b32 v[26:27], v26 offset0:40 offset1:44
	global_load_dwordx4 v[40:43], v24, s[4:5]
	ds_write2st64_b32 v30, v59, v51 offset1:1
	v_lshl_add_u32 v24, v25, 7, v45
	s_waitcnt lgkmcnt(2)
	v_lshl_add_u32 v25, v28, 7, v45
	v_lshl_add_u32 v28, v29, 7, v45
	s_waitcnt lgkmcnt(1)
	v_lshl_add_u32 v26, v26, 7, v45
	v_lshl_add_u32 v27, v27, 7, v45
	global_load_dwordx4 v[62:65], v24, s[4:5]
	global_load_dwordx4 v[36:39], v25, s[4:5]
	global_load_dwordx4 v[32:35], v28, s[4:5]
	s_nop 0
	global_load_dwordx4 v[28:31], v26, s[4:5]
	s_nop 0
	global_load_dwordx4 v[24:27], v27, s[4:5]
	v_cmp_lt_i32_e32 vcc, 48, v57
	s_waitcnt vmcnt(11)
	v_cvt_f32_f16_e32 v70, v10
	v_cvt_f32_f16_sdwa v71, v10 dst_sel:DWORD dst_unused:UNUSED_PAD src0_sel:WORD_1
	v_cvt_f32_f16_e32 v66, v8
	v_cvt_f32_f16_sdwa v67, v8 dst_sel:DWORD dst_unused:UNUSED_PAD src0_sel:WORD_1
	s_waitcnt vmcnt(9)
	s_waitcnt vmcnt(8)
	v_cvt_f32_f16_e32 v84, v22
	v_cvt_f32_f16_sdwa v85, v22 dst_sel:DWORD dst_unused:UNUSED_PAD src0_sel:WORD_1
	v_cvt_f32_f16_e32 v91, v23
	v_cvt_f32_f16_e32 v87, v15
	v_cvt_f32_f16_e32 v68, v9
	v_cvt_f32_f16_sdwa v69, v9 dst_sel:DWORD dst_unused:UNUSED_PAD src0_sel:WORD_1
	v_cvt_f32_f16_e32 v72, v12
	v_cvt_f32_f16_sdwa v73, v12 dst_sel:DWORD dst_unused:UNUSED_PAD src0_sel:WORD_1
	s_waitcnt vmcnt(6)
	v_cvt_f32_f16_e32 v78, v1
	v_cvt_f32_f16_sdwa v79, v1 dst_sel:DWORD dst_unused:UNUSED_PAD src0_sel:WORD_1
	v_cvt_f32_f16_sdwa v1, v23 dst_sel:DWORD dst_unused:UNUSED_PAD src0_sel:WORD_1
	ds_read2_b32 v[22:23], v60 offset1:4
	v_cvt_f32_f16_e32 v61, v11
	v_cvt_f32_f16_sdwa v9, v15 dst_sel:DWORD dst_unused:UNUSED_PAD src0_sel:WORD_1
	v_cvt_f32_f16_sdwa v8, v11 dst_sel:DWORD dst_unused:UNUSED_PAD src0_sel:WORD_1
	s_waitcnt lgkmcnt(0)
	v_mov_b32_e32 v86, v23
	v_pk_fma_f32 v[70:71], v[22:23], v[70:71], 0 op_sel_hi:[0,1,0]
	v_fma_mix_f32 v70, v86, v14, v70 op_sel_hi:[0,1,0]
	v_fma_mix_f32 v71, v86, v14, v71 op_sel:[0,1,0] op_sel_hi:[0,1,0]
	ds_read2_b32 v[74:75], v60 offset0:8 offset1:12
	v_cvt_f32_f16_e32 v10, v4
	v_cvt_f32_f16_sdwa v11, v4 dst_sel:DWORD dst_unused:UNUSED_PAD src0_sel:WORD_1
	v_cvt_f32_f16_e32 v14, v5
	v_cvt_f32_f16_sdwa v15, v5 dst_sel:DWORD dst_unused:UNUSED_PAD src0_sel:WORD_1
	v_cvt_f32_f16_e32 v88, v7
	v_cvt_f32_f16_sdwa v4, v7 dst_sel:DWORD dst_unused:UNUSED_PAD src0_sel:WORD_1
	v_pk_fma_f32 v[68:69], v[22:23], v[68:69], 0 op_sel_hi:[0,1,0]
	v_pk_fma_f32 v[66:67], v[22:23], v[66:67], 0 op_sel_hi:[0,1,0]
	v_fma_mix_f32 v12, v86, v13, v68 op_sel_hi:[0,1,0]
	v_fma_mix_f32 v13, v86, v13, v69 op_sel:[0,1,0] op_sel_hi:[0,1,0]
	v_pk_fma_f32 v[66:67], v[86:87], v[72:73], v[66:67] op_sel_hi:[0,1,1]
	s_waitcnt lgkmcnt(0)
	v_pk_fma_f32 v[10:11], v[74:75], v[10:11], v[66:67] op_sel_hi:[0,1,1]
	v_pk_fma_f32 v[12:13], v[74:75], v[14:15], v[12:13] op_sel_hi:[0,1,1]
	v_mov_b32_e32 v14, v75
	v_fma_mix_f32 v66, v74, v6, v70 op_sel_hi:[0,1,0]
	v_fma_mix_f32 v67, v74, v6, v71 op_sel:[0,1,0] op_sel_hi:[0,1,0]
	v_fma_mix_f32 v66, v14, v2, v66 op_sel_hi:[0,1,0]
	v_fma_mix_f32 v67, v14, v2, v67 op_sel:[0,1,0] op_sel_hi:[0,1,0]
	v_pk_fma_f32 v[12:13], v[14:15], v[78:79], v[12:13] op_sel_hi:[0,1,1]
	v_fma_mix_f32 v6, v14, v0, v10 op_sel_hi:[0,1,0]
	v_fma_mix_f32 v7, v14, v0, v11 op_sel:[0,1,0] op_sel_hi:[0,1,0]
	s_waitcnt vmcnt(5)
	v_cvt_f32_f16_e32 v10, v40
	v_cvt_f32_f16_sdwa v11, v40 dst_sel:DWORD dst_unused:UNUSED_PAD src0_sel:WORD_1
	v_cvt_f32_f16_e32 v14, v41
	v_cvt_f32_f16_sdwa v15, v41 dst_sel:DWORD dst_unused:UNUSED_PAD src0_sel:WORD_1
	ds_read2_b32 v[40:41], v60 offset0:16 offset1:20
	v_cvt_f32_f16_e32 v89, v3
	v_cvt_f32_f16_sdwa v5, v3 dst_sel:DWORD dst_unused:UNUSED_PAD src0_sel:WORD_1
	v_cvt_f32_f16_e32 v2, v16
	v_cvt_f32_f16_sdwa v3, v16 dst_sel:DWORD dst_unused:UNUSED_PAD src0_sel:WORD_1
	v_cvt_f32_f16_e32 v16, v17
	v_cvt_f32_f16_sdwa v17, v17 dst_sel:DWORD dst_unused:UNUSED_PAD src0_sel:WORD_1
	v_cvt_f32_f16_e32 v90, v19
	v_cvt_f32_f16_e32 v82, v18
	v_cvt_f32_f16_sdwa v83, v18 dst_sel:DWORD dst_unused:UNUSED_PAD src0_sel:WORD_1
	v_cvt_f32_f16_sdwa v0, v19 dst_sel:DWORD dst_unused:UNUSED_PAD src0_sel:WORD_1
	s_waitcnt lgkmcnt(0)
	v_pk_fma_f32 v[2:3], v[40:41], v[2:3], v[6:7] op_sel_hi:[0,1,1]
	v_pk_fma_f32 v[6:7], v[40:41], v[16:17], v[12:13] op_sel_hi:[0,1,1]
	v_mov_b32_e32 v16, v41
	v_fma_mix_f32 v2, v16, v20, v2 op_sel_hi:[0,1,0]
	v_fma_mix_f32 v3, v16, v20, v3 op_sel:[0,1,0] op_sel_hi:[0,1,0]
	ds_read2_b32 v[18:19], v60 offset0:24 offset1:28
	v_pk_fma_f32 v[12:13], v[40:41], v[82:83], v[66:67] op_sel_hi:[0,1,1]
	v_pk_fma_f32 v[12:13], v[16:17], v[84:85], v[12:13] op_sel_hi:[0,1,1]
	v_fma_mix_f32 v6, v16, v21, v6 op_sel_hi:[0,1,0]
	v_fma_mix_f32 v7, v16, v21, v7 op_sel:[0,1,0] op_sel_hi:[0,1,0]
	s_waitcnt vmcnt(4)
	v_cvt_f32_f16_e32 v20, v62
	v_cvt_f32_f16_sdwa v21, v62 dst_sel:DWORD dst_unused:UNUSED_PAD src0_sel:WORD_1
	v_cvt_f32_f16_e32 v16, v63
	v_cvt_f32_f16_sdwa v17, v63 dst_sel:DWORD dst_unused:UNUSED_PAD src0_sel:WORD_1
	v_pk_mul_f32 v[8:9], v[22:23], v[8:9]
	s_waitcnt lgkmcnt(0)
	v_pk_fma_f32 v[2:3], v[18:19], v[10:11], v[2:3] op_sel_hi:[0,1,1]
	v_fma_mix_f32 v10, v18, v42, v12 op_sel_hi:[0,1,0]
	v_fma_mix_f32 v11, v18, v42, v13 op_sel:[0,1,0] op_sel_hi:[0,1,0]
	v_mov_b32_e32 v12, v19
	s_waitcnt vmcnt(0)
	v_cvt_f32_f16_e32 v66, v26
	v_cvt_f32_f16_sdwa v67, v26 dst_sel:DWORD dst_unused:UNUSED_PAD src0_sel:WORD_1
	v_mul_f32_e32 v22, v22, v61
	v_mul_f32_e32 v26, v23, v87
	v_mov_b32_e32 v23, v8
	v_fma_mix_f32 v10, v12, v64, v10 op_sel_hi:[0,1,0]
	v_fma_mix_f32 v11, v12, v64, v11 op_sel:[0,1,0] op_sel_hi:[0,1,0]
	v_cvt_f32_f16_e32 v62, v30
	v_cvt_f32_f16_sdwa v63, v30 dst_sel:DWORD dst_unused:UNUSED_PAD src0_sel:WORD_1
	v_cvt_f32_f16_e32 v72, v31
	v_cvt_f32_f16_sdwa v30, v31 dst_sel:DWORD dst_unused:UNUSED_PAD src0_sel:WORD_1
	v_cvt_f32_f16_sdwa v31, v27 dst_sel:DWORD dst_unused:UNUSED_PAD src0_sel:WORD_1
	v_cvt_f32_f16_e32 v73, v27
	v_mov_b32_e32 v27, v9
	v_pk_add_f32 v[8:9], v[22:23], 0 op_sel_hi:[1,0]
	v_pk_mul_f32 v[4:5], v[74:75], v[4:5]
	v_pk_add_f32 v[8:9], v[8:9], v[26:27]
	v_mul_f32_e32 v22, v74, v88
	v_mov_b32_e32 v23, v4
	v_pk_add_f32 v[8:9], v[8:9], v[22:23]
	v_mul_f32_e32 v4, v75, v89
	v_pk_mul_f32 v[0:1], v[40:41], v[0:1]
	v_pk_add_f32 v[4:5], v[8:9], v[4:5]
	v_mul_f32_e32 v8, v40, v90
	v_mov_b32_e32 v9, v0
	v_pk_add_f32 v[4:5], v[4:5], v[8:9]
	v_mul_f32_e32 v0, v41, v91
	v_pk_fma_f32 v[6:7], v[18:19], v[14:15], v[6:7] op_sel_hi:[0,1,1]
	v_pk_add_f32 v[0:1], v[4:5], v[0:1]
	ds_read2_b32 v[4:5], v60 offset0:32 offset1:36
	v_pk_fma_f32 v[6:7], v[12:13], v[16:17], v[6:7] op_sel_hi:[0,1,1]
	v_pk_fma_f32 v[2:3], v[12:13], v[20:21], v[2:3] op_sel_hi:[0,1,1]
	v_cvt_f32_f16_e32 v70, v43
	v_cvt_f32_f16_sdwa v42, v43 dst_sel:DWORD dst_unused:UNUSED_PAD src0_sel:WORD_1
	v_cvt_f32_f16_sdwa v43, v65 dst_sel:DWORD dst_unused:UNUSED_PAD src0_sel:WORD_1
	v_cvt_f32_f16_e32 v71, v65
	v_cvt_f32_f16_sdwa v20, v39 dst_sel:DWORD dst_unused:UNUSED_PAD src0_sel:WORD_1
	v_cvt_f32_f16_sdwa v21, v35 dst_sel:DWORD dst_unused:UNUSED_PAD src0_sel:WORD_1
	v_cvt_f32_f16_e32 v68, v39
	s_waitcnt lgkmcnt(0)
	v_fma_mix_f32 v2, v4, v36, v2 op_sel_hi:[0,1,0]
	v_fma_mix_f32 v3, v4, v36, v3 op_sel:[0,1,0] op_sel_hi:[0,1,0]
	ds_read2_b32 v[12:13], v60 offset0:40 offset1:44
	v_cvt_f32_f16_e32 v69, v35
	v_pk_mul_f32 v[8:9], v[18:19], v[42:43]
	v_mul_f32_e32 v22, v18, v70
	v_mov_b32_e32 v23, v8
	v_pk_add_f32 v[0:1], v[0:1], v[22:23]
	v_mul_f32_e32 v8, v19, v71
	v_pk_mul_f32 v[18:19], v[4:5], v[20:21]
	v_cvt_f32_f16_e32 v64, v24
	v_cvt_f32_f16_sdwa v65, v24 dst_sel:DWORD dst_unused:UNUSED_PAD src0_sel:WORD_1
	v_cvt_f32_f16_e32 v24, v25
	v_cvt_f32_f16_sdwa v25, v25 dst_sel:DWORD dst_unused:UNUSED_PAD src0_sel:WORD_1
	v_fma_mix_f32 v6, v4, v37, v6 op_sel_hi:[0,1,0]
	v_fma_mix_f32 v7, v4, v37, v7 op_sel:[0,1,0] op_sel_hi:[0,1,0]
	v_mul_f32_e32 v14, v4, v68
	v_pk_add_f32 v[0:1], v[0:1], v[8:9]
	v_mov_b32_e32 v15, v18
	v_fma_mix_f32 v10, v4, v38, v10 op_sel_hi:[0,1,0]
	v_fma_mix_f32 v11, v4, v38, v11 op_sel:[0,1,0] op_sel_hi:[0,1,0]
	v_mul_f32_e32 v16, v5, v69
	v_mov_b32_e32 v20, v5
	s_waitcnt lgkmcnt(0)
	v_pk_mul_f32 v[26:27], v[12:13], v[30:31]
	v_pk_add_f32 v[0:1], v[0:1], v[14:15]
	v_mov_b32_e32 v17, v19
	v_mul_f32_e32 v4, v12, v72
	v_fma_mix_f32 v10, v20, v34, v10 op_sel_hi:[0,1,0]
	v_fma_mix_f32 v11, v20, v34, v11 op_sel:[0,1,0] op_sel_hi:[0,1,0]
	v_fma_mix_f32 v6, v20, v33, v6 op_sel_hi:[0,1,0]
	v_fma_mix_f32 v7, v20, v33, v7 op_sel:[0,1,0] op_sel_hi:[0,1,0]
	v_fma_mix_f32 v2, v20, v32, v2 op_sel_hi:[0,1,0]
	v_fma_mix_f32 v3, v20, v32, v3 op_sel:[0,1,0] op_sel_hi:[0,1,0]
	v_pk_add_f32 v[0:1], v[0:1], v[16:17]
	v_mov_b32_e32 v5, v26
	v_mov_b32_e32 v22, v13
	v_mul_f32_e32 v8, v13, v73
	v_pk_add_f32 v[14:15], v[0:1], v[4:5]
	v_fma_mix_f32 v0, v12, v28, v2 op_sel_hi:[0,1,0]
	v_fma_mix_f32 v1, v12, v28, v3 op_sel:[0,1,0] op_sel_hi:[0,1,0]
	v_fma_mix_f32 v2, v12, v29, v6 op_sel_hi:[0,1,0]
	v_fma_mix_f32 v3, v12, v29, v7 op_sel:[0,1,0] op_sel_hi:[0,1,0]
	v_pk_fma_f32 v[4:5], v[12:13], v[62:63], v[10:11] op_sel_hi:[0,1,1]
	v_mov_b32_e32 v9, v27
	v_pk_fma_f32 v[4:5], v[22:23], v[66:67], v[4:5] op_sel_hi:[0,1,1]
	v_pk_fma_f32 v[2:3], v[22:23], v[24:25], v[2:3] op_sel_hi:[0,1,1]
	v_pk_fma_f32 v[0:1], v[22:23], v[64:65], v[0:1] op_sel_hi:[0,1,1]
	v_pk_add_f32 v[6:7], v[14:15], v[8:9]
	s_and_saveexec_b64 s[8:9], vcc
	s_cbranch_execz .LBB4_17
	s_movk_i32 s10, 0x8c0
	v_or3_b32 v24, v58, v50, s10
	s_mov_b64 s[10:11], 0
.LBB4_15:
	ds_read2_b32 v[8:9], v24 offset1:4
	ds_read2_b32 v[10:11], v24 offset0:8 offset1:12
	s_add_i32 s3, s3, 16
	v_cmp_ge_i32_e32 vcc, s3, v57
	s_or_b64 s[10:11], vcc, s[10:11]
	s_waitcnt lgkmcnt(1)
	v_lshl_add_u32 v25, v8, 7, v45
	v_lshl_add_u32 v26, v9, 7, v45
	s_waitcnt lgkmcnt(0)
	v_lshl_add_u32 v27, v10, 7, v45
	v_lshl_add_u32 v28, v11, 7, v45
	global_load_dwordx4 v[20:23], v25, s[4:5]
	global_load_dwordx4 v[16:19], v26, s[4:5]
	global_load_dwordx4 v[8:11], v27, s[4:5]
	global_load_dwordx4 v[12:15], v28, s[4:5]
	v_add_u32_e32 v25, 0x800, v24
	ds_read2_b32 v[26:27], v25 offset1:4
	ds_read2_b32 v[28:29], v25 offset0:8 offset1:12
	v_add_u32_e32 v24, 64, v24
	s_waitcnt lgkmcnt(1)
	v_mov_b32_e32 v30, v27
	s_waitcnt lgkmcnt(0)
	v_mov_b32_e32 v32, v29
	s_waitcnt vmcnt(3)
	v_cvt_f32_f16_sdwa v34, v23 dst_sel:DWORD dst_unused:UNUSED_PAD src0_sel:WORD_1
	s_waitcnt vmcnt(2)
	v_cvt_f32_f16_sdwa v35, v19 dst_sel:DWORD dst_unused:UNUSED_PAD src0_sel:WORD_1
	v_cvt_f32_f16_e32 v25, v23
	v_cvt_f32_f16_e32 v31, v19
	v_cvt_f32_f16_e32 v60, v22
	v_cvt_f32_f16_sdwa v61, v22 dst_sel:DWORD dst_unused:UNUSED_PAD src0_sel:WORD_1
	s_waitcnt vmcnt(0)
	v_cvt_f32_f16_e32 v62, v14
	v_cvt_f32_f16_sdwa v63, v14 dst_sel:DWORD dst_unused:UNUSED_PAD src0_sel:WORD_1
	v_cvt_f32_f16_e32 v50, v15
	v_cvt_f32_f16_sdwa v15, v15 dst_sel:DWORD dst_unused:UNUSED_PAD src0_sel:WORD_1
	v_cvt_f32_f16_sdwa v14, v11 dst_sel:DWORD dst_unused:UNUSED_PAD src0_sel:WORD_1
	v_cvt_f32_f16_e32 v33, v11
	v_cvt_f32_f16_e32 v22, v18
	v_cvt_f32_f16_sdwa v23, v18 dst_sel:DWORD dst_unused:UNUSED_PAD src0_sel:WORD_1
	v_cvt_f32_f16_e32 v18, v10
	v_cvt_f32_f16_sdwa v19, v10 dst_sel:DWORD dst_unused:UNUSED_PAD src0_sel:WORD_1
	v_pk_mul_f32 v[34:35], v[26:27], v[34:35]
	v_cvt_f32_f16_e32 v42, v12
	v_cvt_f32_f16_sdwa v43, v12 dst_sel:DWORD dst_unused:UNUSED_PAD src0_sel:WORD_1
	v_mul_f32_e32 v10, v26, v25
	v_mov_b32_e32 v11, v34
	v_mul_f32_e32 v64, v27, v31
	v_pk_mul_f32 v[14:15], v[28:29], v[14:15]
	v_fma_mix_f32 v0, v26, v20, v0 op_sel_hi:[0,1,0]
	v_fma_mix_f32 v1, v26, v20, v1 op_sel:[0,1,0] op_sel_hi:[0,1,0]
	v_fma_mix_f32 v2, v26, v21, v2 op_sel_hi:[0,1,0]
	v_fma_mix_f32 v3, v26, v21, v3 op_sel:[0,1,0] op_sel_hi:[0,1,0]
	v_pk_fma_f32 v[4:5], v[26:27], v[60:61], v[4:5] op_sel_hi:[0,1,1]
	v_mov_b32_e32 v65, v35
	v_pk_add_f32 v[6:7], v[6:7], v[10:11]
	v_mul_f32_e32 v66, v28, v33
	v_pk_fma_f32 v[4:5], v[30:31], v[22:23], v[4:5] op_sel_hi:[0,1,1]
	v_fma_mix_f32 v2, v30, v17, v2 op_sel_hi:[0,1,0]
	v_fma_mix_f32 v3, v30, v17, v3 op_sel:[0,1,0] op_sel_hi:[0,1,0]
	v_fma_mix_f32 v0, v30, v16, v0 op_sel_hi:[0,1,0]
	v_fma_mix_f32 v1, v30, v16, v1 op_sel:[0,1,0] op_sel_hi:[0,1,0]
	v_mov_b32_e32 v67, v14
	v_pk_add_f32 v[6:7], v[6:7], v[64:65]
	v_mul_f32_e32 v68, v29, v50
	v_mov_b32_e32 v69, v15
	v_fma_mix_f32 v0, v28, v8, v0 op_sel_hi:[0,1,0]
	v_fma_mix_f32 v1, v28, v8, v1 op_sel:[0,1,0] op_sel_hi:[0,1,0]
	v_fma_mix_f32 v2, v28, v9, v2 op_sel_hi:[0,1,0]
	v_fma_mix_f32 v3, v28, v9, v3 op_sel:[0,1,0] op_sel_hi:[0,1,0]
	v_pk_fma_f32 v[4:5], v[28:29], v[18:19], v[4:5] op_sel_hi:[0,1,1]
	v_pk_add_f32 v[6:7], v[6:7], v[66:67]
	v_pk_fma_f32 v[4:5], v[32:33], v[62:63], v[4:5] op_sel_hi:[0,1,1]
	v_fma_mix_f32 v2, v32, v13, v2 op_sel_hi:[0,1,0]
	v_fma_mix_f32 v3, v32, v13, v3 op_sel:[0,1,0] op_sel_hi:[0,1,0]
	v_pk_fma_f32 v[0:1], v[32:33], v[42:43], v[0:1] op_sel_hi:[0,1,1]
	v_pk_add_f32 v[6:7], v[6:7], v[68:69]
	s_andn2_b64 exec, exec, s[10:11]
	s_cbranch_execnz .LBB4_15
	s_or_b64 exec, exec, s[10:11]
